# MoE1: expert bias rows loaded at unit start (before the K-loop) instead of in the epilogue behind a vmcnt(0); swiglu epilogue with 12 temps
# speedup vs baseline: 1.0213x; 1.0012x over previous
.LBB0_2070:
	s_ashr_i32 s19, s18, 31
	s_lshl_b64 s[36:37], s[18:19], 23
	v_readlane_b32 s17, v237, 42
	s_add_u32 s19, s17, s36
	v_readlane_b32 s17, v237, 43
	s_addc_u32 s58, s17, s37
	s_ashr_i32 s17, s16, 31
	s_lshl_b64 s[36:37], s[16:17], 19
	s_add_u32 s36, s19, s36
	s_addc_u32 s37, s58, s37
	s_and_b64 s[58:59], s[54:55], exec
	s_cselect_b32 s17, s37, s57
	s_cselect_b32 s19, s36, s56
	s_add_u32 s58, s56, 0x100
	v_mov_b32_e32 v66, 0
	v_mov_b32_e32 v209, v201
	v_mov_b32_e32 v211, v201
	s_addc_u32 s59, s57, 0
	s_mov_b32 s84, -2
	s_mov_b64 s[56:57], s[24:25]
	v_mov_b32_e32 v67, v66
	v_mov_b32_e32 v68, v66
	v_mov_b32_e32 v69, v66
	v_mov_b32_e32 v74, v66
	v_mov_b32_e32 v75, v66
	v_mov_b32_e32 v76, v66
	v_mov_b32_e32 v77, v66
	v_mov_b32_e32 v82, v66
	v_mov_b32_e32 v83, v66
	v_mov_b32_e32 v84, v66
	v_mov_b32_e32 v85, v66
	v_mov_b32_e32 v90, v66
	v_mov_b32_e32 v91, v66
	v_mov_b32_e32 v92, v66
	v_mov_b32_e32 v93, v66
	v_mov_b32_e32 v98, v66
	v_mov_b32_e32 v99, v66
	v_mov_b32_e32 v100, v66
	v_mov_b32_e32 v101, v66
	v_mov_b32_e32 v106, v66
	v_mov_b32_e32 v107, v66
	v_mov_b32_e32 v108, v66
	v_mov_b32_e32 v109, v66
	v_mov_b32_e32 v114, v66
	v_mov_b32_e32 v115, v66
	v_mov_b32_e32 v116, v66
	v_mov_b32_e32 v117, v66
	v_mov_b32_e32 v122, v66
	v_mov_b32_e32 v123, v66
	v_mov_b32_e32 v124, v66
	v_mov_b32_e32 v125, v66
	v_mov_b32_e32 v70, v66
	v_mov_b32_e32 v71, v66
	v_mov_b32_e32 v72, v66
	v_mov_b32_e32 v73, v66
	v_mov_b32_e32 v78, v66
	v_mov_b32_e32 v79, v66
	v_mov_b32_e32 v80, v66
	v_mov_b32_e32 v81, v66
	v_mov_b32_e32 v86, v66
	v_mov_b32_e32 v87, v66
	v_mov_b32_e32 v88, v66
	v_mov_b32_e32 v89, v66
	v_mov_b32_e32 v94, v66
	v_mov_b32_e32 v95, v66
	v_mov_b32_e32 v96, v66
	v_mov_b32_e32 v97, v66
	v_mov_b32_e32 v102, v66
	v_mov_b32_e32 v103, v66
	v_mov_b32_e32 v104, v66
	v_mov_b32_e32 v105, v66
	v_mov_b32_e32 v110, v66
	v_mov_b32_e32 v111, v66
	v_mov_b32_e32 v112, v66
	v_mov_b32_e32 v113, v66
	v_mov_b32_e32 v118, v66
	v_mov_b32_e32 v119, v66
	v_mov_b32_e32 v120, v66
	v_mov_b32_e32 v121, v66
	v_mov_b32_e32 v126, v66
	v_mov_b32_e32 v127, v66
	v_mov_b32_e32 v128, v66
	v_mov_b32_e32 v129, v66
	v_mov_b32_e32 v130, v66
	v_mov_b32_e32 v131, v66
	v_mov_b32_e32 v132, v66
	v_mov_b32_e32 v133, v66
	v_mov_b32_e32 v138, v66
	v_mov_b32_e32 v139, v66
	v_mov_b32_e32 v140, v66
	v_mov_b32_e32 v141, v66
	v_mov_b32_e32 v146, v66
	v_mov_b32_e32 v147, v66
	v_mov_b32_e32 v148, v66
	v_mov_b32_e32 v149, v66
	v_mov_b32_e32 v154, v66
	v_mov_b32_e32 v155, v66
	v_mov_b32_e32 v156, v66
	v_mov_b32_e32 v157, v66
	v_mov_b32_e32 v162, v66
	v_mov_b32_e32 v163, v66
	v_mov_b32_e32 v164, v66
	v_mov_b32_e32 v165, v66
	v_mov_b32_e32 v170, v66
	v_mov_b32_e32 v171, v66
	v_mov_b32_e32 v172, v66
	v_mov_b32_e32 v173, v66
	v_mov_b32_e32 v178, v66
	v_mov_b32_e32 v179, v66
	v_mov_b32_e32 v180, v66
	v_mov_b32_e32 v181, v66
	v_mov_b32_e32 v186, v66
	v_mov_b32_e32 v187, v66
	v_mov_b32_e32 v188, v66
	v_mov_b32_e32 v189, v66
	v_mov_b32_e32 v134, v66
	v_mov_b32_e32 v135, v66
	v_mov_b32_e32 v136, v66
	v_mov_b32_e32 v137, v66
	v_mov_b32_e32 v142, v66
	v_mov_b32_e32 v143, v66
	v_mov_b32_e32 v144, v66
	v_mov_b32_e32 v145, v66
	v_mov_b32_e32 v150, v66
	v_mov_b32_e32 v151, v66
	v_mov_b32_e32 v152, v66
	v_mov_b32_e32 v153, v66
	v_mov_b32_e32 v158, v66
	v_mov_b32_e32 v159, v66
	v_mov_b32_e32 v160, v66
	v_mov_b32_e32 v161, v66
	v_mov_b32_e32 v166, v66
	v_mov_b32_e32 v167, v66
	v_mov_b32_e32 v168, v66
	v_mov_b32_e32 v169, v66
	v_mov_b32_e32 v174, v66
	v_mov_b32_e32 v175, v66
	v_mov_b32_e32 v176, v66
	v_mov_b32_e32 v177, v66
	v_mov_b32_e32 v182, v66
	v_mov_b32_e32 v183, v66
	v_mov_b32_e32 v184, v66
	v_mov_b32_e32 v185, v66
	v_mov_b32_e32 v190, v66
	v_mov_b32_e32 v191, v66
	v_mov_b32_e32 v192, v66
	v_mov_b32_e32 v193, v66
	v_lshl_or_b32 v254, s53, 7, v219
	s_mov_b32 s98, s52
	s_ashr_i32 s99, s52, 31
	s_lshl_b64 s[98:99], s[98:99], 14
	s_add_u32 s98, s40, s98
	s_addc_u32 s99, s41, s99
	v_ashrrev_i32_e32 v255, 31, v254
	v_lshl_add_u64 v[254:255], v[254:255], 2, s[98:99]
	global_load_dwordx4 v[238:241], v[254:255], off
	global_load_dwordx4 v[242:245], v[254:255], off offset:16
	v_lshl_add_u64 v[254:255], v[254:255], 0, s[42:43]
	global_load_dwordx4 v[246:249], v[254:255], off
	global_load_dwordx4 v[250:253], v[254:255], off offset:16
	s_branch .LBB0_2073

.LBB0_2077:
	v_lshl_or_b32 v20, s53, 7, v219
	v_ashrrev_i32_e32 v21, 31, v20
	s_nop 15
	s_nop 15
	s_nop 15
	s_nop 15
	v_lshl_add_u32 v22, s83, 8, v217
	s_nop 0
	s_mov_b32 s90, 0x3c800000
	s_mov_b32 s92, 0xc01d265f
	s_mov_b32 s94, 0x3fb8aa3b
	s_mov_b32 s96, 1.0
	v_pk_fma_f32 v[28:29], v[190:191], s[90:91], v[238:239] op_sel_hi:[1,0,1]
	v_pk_fma_f32 v[30:31], v[192:193], s[90:91], v[240:241] op_sel_hi:[1,0,1]
	v_min_f32_e32 v28, 0x40e00000, v28
	v_min_f32_e32 v29, 0x40e00000, v29
	v_min_f32_e32 v30, 0x40e00000, v30
	v_min_f32_e32 v31, 0x40e00000, v31
	v_pk_mul_f32 v[32:33], v[28:29], s[92:93] op_sel_hi:[1,0]
	v_pk_mul_f32 v[34:35], v[30:31], s[92:93] op_sel_hi:[1,0]
	v_exp_f32_e32 v32, v32
	v_exp_f32_e32 v33, v33
	v_exp_f32_e32 v34, v34
	v_exp_f32_e32 v35, v35
	v_pk_add_f32 v[32:33], v[32:33], s[96:97] op_sel_hi:[1,0]
	v_pk_add_f32 v[34:35], v[34:35], s[96:97] op_sel_hi:[1,0]
	v_rcp_f32_e32 v32, v32
	v_rcp_f32_e32 v33, v33
	v_rcp_f32_e32 v34, v34
	v_rcp_f32_e32 v35, v35
	v_pk_mul_f32 v[28:29], v[28:29], v[32:33]
	v_pk_mul_f32 v[30:31], v[30:31], v[34:35]
	v_pk_fma_f32 v[32:33], v[186:187], s[90:91], v[246:247] op_sel_hi:[1,0,1]
	v_pk_fma_f32 v[34:35], v[188:189], s[90:91], v[248:249] op_sel_hi:[1,0,1]
	v_med3_f32 v32, v32, s79, v224
	v_med3_f32 v33, v33, s79, v224
	v_med3_f32 v34, v34, s79, v224
	v_med3_f32 v35, v35, s79, v224
	v_fma_f32 v32, v32, 4.0, 4.0
	v_fma_f32 v33, v33, 4.0, 4.0
	v_fma_f32 v34, v34, 4.0, 4.0
	v_fma_f32 v35, v35, 4.0, 4.0
	v_pk_mul_f32 v[28:29], v[32:33], v[28:29]
	v_pk_mul_f32 v[30:31], v[34:35], v[30:31]
	v_pk_fma_f32 v[36:37], v[182:183], s[90:91], v[242:243] op_sel_hi:[1,0,1]
	v_pk_fma_f32 v[38:39], v[184:185], s[90:91], v[244:245] op_sel_hi:[1,0,1]
	v_min_f32_e32 v36, 0x40e00000, v36
	v_min_f32_e32 v37, 0x40e00000, v37
	v_min_f32_e32 v38, 0x40e00000, v38
	v_min_f32_e32 v39, 0x40e00000, v39
	v_pk_mul_f32 v[32:33], v[36:37], s[92:93] op_sel_hi:[1,0]
	v_pk_mul_f32 v[34:35], v[38:39], s[92:93] op_sel_hi:[1,0]
	v_exp_f32_e32 v32, v32
	v_exp_f32_e32 v33, v33
	v_exp_f32_e32 v34, v34
	v_exp_f32_e32 v35, v35
	v_pk_add_f32 v[32:33], v[32:33], s[96:97] op_sel_hi:[1,0]
	v_pk_add_f32 v[34:35], v[34:35], s[96:97] op_sel_hi:[1,0]
	v_rcp_f32_e32 v32, v32
	v_rcp_f32_e32 v33, v33
	v_rcp_f32_e32 v34, v34
	v_rcp_f32_e32 v35, v35
	v_pk_mul_f32 v[36:37], v[36:37], v[32:33]
	v_pk_mul_f32 v[38:39], v[38:39], v[34:35]
	v_pk_fma_f32 v[32:33], v[178:179], s[90:91], v[250:251] op_sel_hi:[1,0,1]
	v_pk_fma_f32 v[34:35], v[180:181], s[90:91], v[252:253] op_sel_hi:[1,0,1]
	v_med3_f32 v32, v32, s79, v224
	v_med3_f32 v33, v33, s79, v224
	v_med3_f32 v34, v34, s79, v224
	v_med3_f32 v35, v35, s79, v224
	v_fma_f32 v32, v32, 4.0, 4.0
	v_fma_f32 v33, v33, 4.0, 4.0
	v_fma_f32 v34, v34, 4.0, 4.0
	v_fma_f32 v35, v35, 4.0, 4.0
	v_pk_mul_f32 v[36:37], v[32:33], v[36:37]
	v_pk_mul_f32 v[38:39], v[34:35], v[38:39]
	v_ashrrev_i32_e32 v23, 31, v22
	v_lshlrev_b64 v[18:19], 11, v[22:23]
	v_lshl_add_u64 v[18:19], s[6:7], 0, v[18:19]
	v_lshl_add_u64 v[18:19], v[18:19], 0, v[20:21]
	v_mov_b32_e32 v24, v201
	v_mov_b32_e32 v25, v201
	v_cvt_pk_fp8_f32 v24, v28, v29
	v_cvt_pk_fp8_f32 v25, v36, v37
	v_cvt_pk_fp8_f32 v24, v30, v31 op_sel:[0,0,1]
	v_cvt_pk_fp8_f32 v25, v38, v39 op_sel:[0,0,1]
	global_store_dwordx2 v[18:19], v[24:25], off
	v_pk_fma_f32 v[28:29], v[174:175], s[90:91], v[238:239] op_sel_hi:[1,0,1]
	v_pk_fma_f32 v[30:31], v[176:177], s[90:91], v[240:241] op_sel_hi:[1,0,1]
	v_min_f32_e32 v28, 0x40e00000, v28
	v_min_f32_e32 v29, 0x40e00000, v29
	v_min_f32_e32 v30, 0x40e00000, v30
	v_min_f32_e32 v31, 0x40e00000, v31
	v_pk_mul_f32 v[32:33], v[28:29], s[92:93] op_sel_hi:[1,0]
	v_pk_mul_f32 v[34:35], v[30:31], s[92:93] op_sel_hi:[1,0]
	v_exp_f32_e32 v32, v32
	v_exp_f32_e32 v33, v33
	v_exp_f32_e32 v34, v34
	v_exp_f32_e32 v35, v35
	v_pk_add_f32 v[32:33], v[32:33], s[96:97] op_sel_hi:[1,0]
	v_pk_add_f32 v[34:35], v[34:35], s[96:97] op_sel_hi:[1,0]
	v_rcp_f32_e32 v32, v32
	v_rcp_f32_e32 v33, v33
	v_rcp_f32_e32 v34, v34
	v_rcp_f32_e32 v35, v35
	v_pk_mul_f32 v[28:29], v[28:29], v[32:33]
	v_pk_mul_f32 v[30:31], v[30:31], v[34:35]
	v_pk_fma_f32 v[32:33], v[170:171], s[90:91], v[246:247] op_sel_hi:[1,0,1]
	v_pk_fma_f32 v[34:35], v[172:173], s[90:91], v[248:249] op_sel_hi:[1,0,1]
	v_med3_f32 v32, v32, s79, v224
	v_med3_f32 v33, v33, s79, v224
	v_med3_f32 v34, v34, s79, v224
	v_med3_f32 v35, v35, s79, v224
	v_fma_f32 v32, v32, 4.0, 4.0
	v_fma_f32 v33, v33, 4.0, 4.0
	v_fma_f32 v34, v34, 4.0, 4.0
	v_fma_f32 v35, v35, 4.0, 4.0
	v_pk_mul_f32 v[28:29], v[32:33], v[28:29]
	v_pk_mul_f32 v[30:31], v[34:35], v[30:31]
	v_pk_fma_f32 v[36:37], v[166:167], s[90:91], v[242:243] op_sel_hi:[1,0,1]
	v_pk_fma_f32 v[38:39], v[168:169], s[90:91], v[244:245] op_sel_hi:[1,0,1]
	v_min_f32_e32 v36, 0x40e00000, v36
	v_min_f32_e32 v37, 0x40e00000, v37
	v_min_f32_e32 v38, 0x40e00000, v38
	v_min_f32_e32 v39, 0x40e00000, v39
	v_pk_mul_f32 v[32:33], v[36:37], s[92:93] op_sel_hi:[1,0]
	v_pk_mul_f32 v[34:35], v[38:39], s[92:93] op_sel_hi:[1,0]
	v_exp_f32_e32 v32, v32
	v_exp_f32_e32 v33, v33
	v_exp_f32_e32 v34, v34
	v_exp_f32_e32 v35, v35
	v_pk_add_f32 v[32:33], v[32:33], s[96:97] op_sel_hi:[1,0]
	v_pk_add_f32 v[34:35], v[34:35], s[96:97] op_sel_hi:[1,0]
	v_rcp_f32_e32 v32, v32
	v_rcp_f32_e32 v33, v33
	v_rcp_f32_e32 v34, v34
	v_rcp_f32_e32 v35, v35
	v_pk_mul_f32 v[36:37], v[36:37], v[32:33]
	v_pk_mul_f32 v[38:39], v[38:39], v[34:35]
	v_pk_fma_f32 v[32:33], v[162:163], s[90:91], v[250:251] op_sel_hi:[1,0,1]
	v_pk_fma_f32 v[34:35], v[164:165], s[90:91], v[252:253] op_sel_hi:[1,0,1]
	v_med3_f32 v32, v32, s79, v224
	v_med3_f32 v33, v33, s79, v224
	v_med3_f32 v34, v34, s79, v224
	v_med3_f32 v35, v35, s79, v224
	v_fma_f32 v32, v32, 4.0, 4.0
	v_fma_f32 v33, v33, 4.0, 4.0
	v_fma_f32 v34, v34, 4.0, 4.0
	v_fma_f32 v35, v35, 4.0, 4.0
	v_pk_mul_f32 v[36:37], v[32:33], v[36:37]
	v_pk_mul_f32 v[38:39], v[34:35], v[38:39]
	v_or_b32_e32 v26, 16, v22
	v_ashrrev_i32_e32 v27, 31, v26
	v_lshlrev_b64 v[26:27], 11, v[26:27]
	v_lshl_add_u64 v[26:27], s[6:7], 0, v[26:27]
	v_lshl_add_u64 v[26:27], v[26:27], 0, v[20:21]
	v_mov_b32_e32 v24, v201
	v_mov_b32_e32 v25, v201
	v_cvt_pk_fp8_f32 v24, v28, v29
	v_cvt_pk_fp8_f32 v25, v36, v37
	v_cvt_pk_fp8_f32 v24, v30, v31 op_sel:[0,0,1]
	v_cvt_pk_fp8_f32 v25, v38, v39 op_sel:[0,0,1]
	global_store_dwordx2 v[26:27], v[24:25], off
	v_pk_fma_f32 v[28:29], v[158:159], s[90:91], v[238:239] op_sel_hi:[1,0,1]
	v_pk_fma_f32 v[30:31], v[160:161], s[90:91], v[240:241] op_sel_hi:[1,0,1]
	v_min_f32_e32 v28, 0x40e00000, v28
	v_min_f32_e32 v29, 0x40e00000, v29
	v_min_f32_e32 v30, 0x40e00000, v30
	v_min_f32_e32 v31, 0x40e00000, v31
	v_pk_mul_f32 v[32:33], v[28:29], s[92:93] op_sel_hi:[1,0]
	v_pk_mul_f32 v[34:35], v[30:31], s[92:93] op_sel_hi:[1,0]
	v_exp_f32_e32 v32, v32
	v_exp_f32_e32 v33, v33
	v_exp_f32_e32 v34, v34
	v_exp_f32_e32 v35, v35
	v_pk_add_f32 v[32:33], v[32:33], s[96:97] op_sel_hi:[1,0]
	v_pk_add_f32 v[34:35], v[34:35], s[96:97] op_sel_hi:[1,0]
	v_rcp_f32_e32 v32, v32
	v_rcp_f32_e32 v33, v33
	v_rcp_f32_e32 v34, v34
	v_rcp_f32_e32 v35, v35
	v_pk_mul_f32 v[28:29], v[28:29], v[32:33]
	v_pk_mul_f32 v[30:31], v[30:31], v[34:35]
	v_pk_fma_f32 v[32:33], v[154:155], s[90:91], v[246:247] op_sel_hi:[1,0,1]
	v_pk_fma_f32 v[34:35], v[156:157], s[90:91], v[248:249] op_sel_hi:[1,0,1]
	v_med3_f32 v32, v32, s79, v224
	v_med3_f32 v33, v33, s79, v224
	v_med3_f32 v34, v34, s79, v224
	v_med3_f32 v35, v35, s79, v224
	v_fma_f32 v32, v32, 4.0, 4.0
	v_fma_f32 v33, v33, 4.0, 4.0
	v_fma_f32 v34, v34, 4.0, 4.0
	v_fma_f32 v35, v35, 4.0, 4.0
	v_pk_mul_f32 v[28:29], v[32:33], v[28:29]
	v_pk_mul_f32 v[30:31], v[34:35], v[30:31]
	v_pk_fma_f32 v[36:37], v[150:151], s[90:91], v[242:243] op_sel_hi:[1,0,1]
	v_pk_fma_f32 v[38:39], v[152:153], s[90:91], v[244:245] op_sel_hi:[1,0,1]
	v_min_f32_e32 v36, 0x40e00000, v36
	v_min_f32_e32 v37, 0x40e00000, v37
	v_min_f32_e32 v38, 0x40e00000, v38
	v_min_f32_e32 v39, 0x40e00000, v39
	v_pk_mul_f32 v[32:33], v[36:37], s[92:93] op_sel_hi:[1,0]
	v_pk_mul_f32 v[34:35], v[38:39], s[92:93] op_sel_hi:[1,0]
	v_exp_f32_e32 v32, v32
	v_exp_f32_e32 v33, v33
	v_exp_f32_e32 v34, v34
	v_exp_f32_e32 v35, v35
	v_pk_add_f32 v[32:33], v[32:33], s[96:97] op_sel_hi:[1,0]
	v_pk_add_f32 v[34:35], v[34:35], s[96:97] op_sel_hi:[1,0]
	v_rcp_f32_e32 v32, v32
	v_rcp_f32_e32 v33, v33
	v_rcp_f32_e32 v34, v34
	v_rcp_f32_e32 v35, v35
	v_pk_mul_f32 v[36:37], v[36:37], v[32:33]
	v_pk_mul_f32 v[38:39], v[38:39], v[34:35]
	v_pk_fma_f32 v[32:33], v[146:147], s[90:91], v[250:251] op_sel_hi:[1,0,1]
	v_pk_fma_f32 v[34:35], v[148:149], s[90:91], v[252:253] op_sel_hi:[1,0,1]
	v_med3_f32 v32, v32, s79, v224
	v_med3_f32 v33, v33, s79, v224
	v_med3_f32 v34, v34, s79, v224
	v_med3_f32 v35, v35, s79, v224
	v_fma_f32 v32, v32, 4.0, 4.0
	v_fma_f32 v33, v33, 4.0, 4.0
	v_fma_f32 v34, v34, 4.0, 4.0
	v_fma_f32 v35, v35, 4.0, 4.0
	v_pk_mul_f32 v[36:37], v[32:33], v[36:37]
	v_pk_mul_f32 v[38:39], v[34:35], v[38:39]
	v_or_b32_e32 v26, 32, v22
	v_ashrrev_i32_e32 v27, 31, v26
	v_lshlrev_b64 v[26:27], 11, v[26:27]
	v_lshl_add_u64 v[26:27], s[6:7], 0, v[26:27]
	v_lshl_add_u64 v[26:27], v[26:27], 0, v[20:21]
	v_mov_b32_e32 v24, v201
	v_mov_b32_e32 v25, v201
	v_cvt_pk_fp8_f32 v24, v28, v29
	v_cvt_pk_fp8_f32 v25, v36, v37
	v_cvt_pk_fp8_f32 v24, v30, v31 op_sel:[0,0,1]
	v_cvt_pk_fp8_f32 v25, v38, v39 op_sel:[0,0,1]
	global_store_dwordx2 v[26:27], v[24:25], off
	v_pk_fma_f32 v[28:29], v[142:143], s[90:91], v[238:239] op_sel_hi:[1,0,1]
	v_pk_fma_f32 v[30:31], v[144:145], s[90:91], v[240:241] op_sel_hi:[1,0,1]
	v_min_f32_e32 v28, 0x40e00000, v28
	v_min_f32_e32 v29, 0x40e00000, v29
	v_min_f32_e32 v30, 0x40e00000, v30
	v_min_f32_e32 v31, 0x40e00000, v31
	v_pk_mul_f32 v[32:33], v[28:29], s[92:93] op_sel_hi:[1,0]
	v_pk_mul_f32 v[34:35], v[30:31], s[92:93] op_sel_hi:[1,0]
	v_exp_f32_e32 v32, v32
	v_exp_f32_e32 v33, v33
	v_exp_f32_e32 v34, v34
	v_exp_f32_e32 v35, v35
	v_pk_add_f32 v[32:33], v[32:33], s[96:97] op_sel_hi:[1,0]
	v_pk_add_f32 v[34:35], v[34:35], s[96:97] op_sel_hi:[1,0]
	v_rcp_f32_e32 v32, v32
	v_rcp_f32_e32 v33, v33
	v_rcp_f32_e32 v34, v34
	v_rcp_f32_e32 v35, v35
	v_pk_mul_f32 v[28:29], v[28:29], v[32:33]
	v_pk_mul_f32 v[30:31], v[30:31], v[34:35]
	v_pk_fma_f32 v[32:33], v[138:139], s[90:91], v[246:247] op_sel_hi:[1,0,1]
	v_pk_fma_f32 v[34:35], v[140:141], s[90:91], v[248:249] op_sel_hi:[1,0,1]
	v_med3_f32 v32, v32, s79, v224
	v_med3_f32 v33, v33, s79, v224
	v_med3_f32 v34, v34, s79, v224
	v_med3_f32 v35, v35, s79, v224
	v_fma_f32 v32, v32, 4.0, 4.0
	v_fma_f32 v33, v33, 4.0, 4.0
	v_fma_f32 v34, v34, 4.0, 4.0
	v_fma_f32 v35, v35, 4.0, 4.0
	v_pk_mul_f32 v[28:29], v[32:33], v[28:29]
	v_pk_mul_f32 v[30:31], v[34:35], v[30:31]
	v_pk_fma_f32 v[36:37], v[134:135], s[90:91], v[242:243] op_sel_hi:[1,0,1]
	v_pk_fma_f32 v[38:39], v[136:137], s[90:91], v[244:245] op_sel_hi:[1,0,1]
	v_min_f32_e32 v36, 0x40e00000, v36
	v_min_f32_e32 v37, 0x40e00000, v37
	v_min_f32_e32 v38, 0x40e00000, v38
	v_min_f32_e32 v39, 0x40e00000, v39
	v_pk_mul_f32 v[32:33], v[36:37], s[92:93] op_sel_hi:[1,0]
	v_pk_mul_f32 v[34:35], v[38:39], s[92:93] op_sel_hi:[1,0]
	v_exp_f32_e32 v32, v32
	v_exp_f32_e32 v33, v33
	v_exp_f32_e32 v34, v34
	v_exp_f32_e32 v35, v35
	v_pk_add_f32 v[32:33], v[32:33], s[96:97] op_sel_hi:[1,0]
	v_pk_add_f32 v[34:35], v[34:35], s[96:97] op_sel_hi:[1,0]
	v_rcp_f32_e32 v32, v32
	v_rcp_f32_e32 v33, v33
	v_rcp_f32_e32 v34, v34
	v_rcp_f32_e32 v35, v35
	v_pk_mul_f32 v[36:37], v[36:37], v[32:33]
	v_pk_mul_f32 v[38:39], v[38:39], v[34:35]
	v_pk_fma_f32 v[32:33], v[130:131], s[90:91], v[250:251] op_sel_hi:[1,0,1]
	v_pk_fma_f32 v[34:35], v[132:133], s[90:91], v[252:253] op_sel_hi:[1,0,1]
	v_med3_f32 v32, v32, s79, v224
	v_med3_f32 v33, v33, s79, v224
	v_med3_f32 v34, v34, s79, v224
	v_med3_f32 v35, v35, s79, v224
	v_fma_f32 v32, v32, 4.0, 4.0
	v_fma_f32 v33, v33, 4.0, 4.0
	v_fma_f32 v34, v34, 4.0, 4.0
	v_fma_f32 v35, v35, 4.0, 4.0
	v_pk_mul_f32 v[36:37], v[32:33], v[36:37]
	v_pk_mul_f32 v[38:39], v[34:35], v[38:39]
	v_or_b32_e32 v22, 48, v22
	v_ashrrev_i32_e32 v23, 31, v22
	v_lshlrev_b64 v[22:23], 11, v[22:23]
	v_lshl_add_u64 v[22:23], s[6:7], 0, v[22:23]
	v_lshl_add_u64 v[20:21], v[22:23], 0, v[20:21]
	v_mov_b32_e32 v24, v201
	v_mov_b32_e32 v25, v201
	v_cvt_pk_fp8_f32 v24, v28, v29
	v_cvt_pk_fp8_f32 v25, v36, v37
	v_cvt_pk_fp8_f32 v24, v30, v31 op_sel:[0,0,1]
	v_cvt_pk_fp8_f32 v25, v38, v39 op_sel:[0,0,1]
	global_store_dwordx2 v[20:21], v[24:25], off
	v_pk_fma_f32 v[28:29], v[126:127], s[90:91], v[238:239] op_sel_hi:[1,0,1]
	v_pk_fma_f32 v[30:31], v[128:129], s[90:91], v[240:241] op_sel_hi:[1,0,1]
	v_min_f32_e32 v28, 0x40e00000, v28
	v_min_f32_e32 v29, 0x40e00000, v29
	v_min_f32_e32 v30, 0x40e00000, v30
	v_min_f32_e32 v31, 0x40e00000, v31
	v_pk_mul_f32 v[32:33], v[28:29], s[92:93] op_sel_hi:[1,0]
	v_pk_mul_f32 v[34:35], v[30:31], s[92:93] op_sel_hi:[1,0]
	v_exp_f32_e32 v32, v32
	v_exp_f32_e32 v33, v33
	v_exp_f32_e32 v34, v34
	v_exp_f32_e32 v35, v35
	v_pk_add_f32 v[32:33], v[32:33], s[96:97] op_sel_hi:[1,0]
	v_pk_add_f32 v[34:35], v[34:35], s[96:97] op_sel_hi:[1,0]
	v_rcp_f32_e32 v32, v32
	v_rcp_f32_e32 v33, v33
	v_rcp_f32_e32 v34, v34
	v_rcp_f32_e32 v35, v35
	v_pk_mul_f32 v[28:29], v[28:29], v[32:33]
	v_pk_mul_f32 v[30:31], v[30:31], v[34:35]
	v_pk_fma_f32 v[32:33], v[122:123], s[90:91], v[246:247] op_sel_hi:[1,0,1]
	v_pk_fma_f32 v[34:35], v[124:125], s[90:91], v[248:249] op_sel_hi:[1,0,1]
	v_med3_f32 v32, v32, s79, v224
	v_med3_f32 v33, v33, s79, v224
	v_med3_f32 v34, v34, s79, v224
	v_med3_f32 v35, v35, s79, v224
	v_fma_f32 v32, v32, 4.0, 4.0
	v_fma_f32 v33, v33, 4.0, 4.0
	v_fma_f32 v34, v34, 4.0, 4.0
	v_fma_f32 v35, v35, 4.0, 4.0
	v_pk_mul_f32 v[28:29], v[32:33], v[28:29]
	v_pk_mul_f32 v[30:31], v[34:35], v[30:31]
	v_pk_fma_f32 v[36:37], v[118:119], s[90:91], v[242:243] op_sel_hi:[1,0,1]
	v_pk_fma_f32 v[38:39], v[120:121], s[90:91], v[244:245] op_sel_hi:[1,0,1]
	v_min_f32_e32 v36, 0x40e00000, v36
	v_min_f32_e32 v37, 0x40e00000, v37
	v_min_f32_e32 v38, 0x40e00000, v38
	v_min_f32_e32 v39, 0x40e00000, v39
	v_pk_mul_f32 v[32:33], v[36:37], s[92:93] op_sel_hi:[1,0]
	v_pk_mul_f32 v[34:35], v[38:39], s[92:93] op_sel_hi:[1,0]
	v_exp_f32_e32 v32, v32
	v_exp_f32_e32 v33, v33
	v_exp_f32_e32 v34, v34
	v_exp_f32_e32 v35, v35
	v_pk_add_f32 v[32:33], v[32:33], s[96:97] op_sel_hi:[1,0]
	v_pk_add_f32 v[34:35], v[34:35], s[96:97] op_sel_hi:[1,0]
	v_rcp_f32_e32 v32, v32
	v_rcp_f32_e32 v33, v33
	v_rcp_f32_e32 v34, v34
	v_rcp_f32_e32 v35, v35
	v_pk_mul_f32 v[36:37], v[36:37], v[32:33]
	v_pk_mul_f32 v[38:39], v[38:39], v[34:35]
	v_pk_fma_f32 v[32:33], v[114:115], s[90:91], v[250:251] op_sel_hi:[1,0,1]
	v_pk_fma_f32 v[34:35], v[116:117], s[90:91], v[252:253] op_sel_hi:[1,0,1]
	v_med3_f32 v32, v32, s79, v224
	v_med3_f32 v33, v33, s79, v224
	v_med3_f32 v34, v34, s79, v224
	v_med3_f32 v35, v35, s79, v224
	v_fma_f32 v32, v32, 4.0, 4.0
	v_fma_f32 v33, v33, 4.0, 4.0
	v_fma_f32 v34, v34, 4.0, 4.0
	v_fma_f32 v35, v35, 4.0, 4.0
	v_pk_mul_f32 v[36:37], v[32:33], v[36:37]
	v_pk_mul_f32 v[38:39], v[34:35], v[38:39]
	v_add_co_u32_e32 v22, vcc, s80, v18
	s_nop 0
	v_addc_co_u32_e32 v23, vcc, 0, v19, vcc
	v_mov_b32_e32 v20, v201
	v_mov_b32_e32 v21, v201
	v_cvt_pk_fp8_f32 v20, v28, v29
	v_cvt_pk_fp8_f32 v21, v36, v37
	v_cvt_pk_fp8_f32 v20, v30, v31 op_sel:[0,0,1]
	v_cvt_pk_fp8_f32 v21, v38, v39 op_sel:[0,0,1]
	global_store_dwordx2 v[22:23], v[20:21], off
	v_pk_fma_f32 v[28:29], v[110:111], s[90:91], v[238:239] op_sel_hi:[1,0,1]
	v_pk_fma_f32 v[30:31], v[112:113], s[90:91], v[240:241] op_sel_hi:[1,0,1]
	v_min_f32_e32 v28, 0x40e00000, v28
	v_min_f32_e32 v29, 0x40e00000, v29
	v_min_f32_e32 v30, 0x40e00000, v30
	v_min_f32_e32 v31, 0x40e00000, v31
	v_pk_mul_f32 v[32:33], v[28:29], s[92:93] op_sel_hi:[1,0]
	v_pk_mul_f32 v[34:35], v[30:31], s[92:93] op_sel_hi:[1,0]
	v_exp_f32_e32 v32, v32
	v_exp_f32_e32 v33, v33
	v_exp_f32_e32 v34, v34
	v_exp_f32_e32 v35, v35
	v_pk_add_f32 v[32:33], v[32:33], s[96:97] op_sel_hi:[1,0]
	v_pk_add_f32 v[34:35], v[34:35], s[96:97] op_sel_hi:[1,0]
	v_rcp_f32_e32 v32, v32
	v_rcp_f32_e32 v33, v33
	v_rcp_f32_e32 v34, v34
	v_rcp_f32_e32 v35, v35
	v_pk_mul_f32 v[28:29], v[28:29], v[32:33]
	v_pk_mul_f32 v[30:31], v[30:31], v[34:35]
	v_pk_fma_f32 v[32:33], v[106:107], s[90:91], v[246:247] op_sel_hi:[1,0,1]
	v_pk_fma_f32 v[34:35], v[108:109], s[90:91], v[248:249] op_sel_hi:[1,0,1]
	v_med3_f32 v32, v32, s79, v224
	v_med3_f32 v33, v33, s79, v224
	v_med3_f32 v34, v34, s79, v224
	v_med3_f32 v35, v35, s79, v224
	v_fma_f32 v32, v32, 4.0, 4.0
	v_fma_f32 v33, v33, 4.0, 4.0
	v_fma_f32 v34, v34, 4.0, 4.0
	v_fma_f32 v35, v35, 4.0, 4.0
	v_pk_mul_f32 v[28:29], v[32:33], v[28:29]
	v_pk_mul_f32 v[30:31], v[34:35], v[30:31]
	v_pk_fma_f32 v[36:37], v[102:103], s[90:91], v[242:243] op_sel_hi:[1,0,1]
	v_pk_fma_f32 v[38:39], v[104:105], s[90:91], v[244:245] op_sel_hi:[1,0,1]
	v_min_f32_e32 v36, 0x40e00000, v36
	v_min_f32_e32 v37, 0x40e00000, v37
	v_min_f32_e32 v38, 0x40e00000, v38
	v_min_f32_e32 v39, 0x40e00000, v39
	v_pk_mul_f32 v[32:33], v[36:37], s[92:93] op_sel_hi:[1,0]
	v_pk_mul_f32 v[34:35], v[38:39], s[92:93] op_sel_hi:[1,0]
	v_exp_f32_e32 v32, v32
	v_exp_f32_e32 v33, v33
	v_exp_f32_e32 v34, v34
	v_exp_f32_e32 v35, v35
	v_pk_add_f32 v[32:33], v[32:33], s[96:97] op_sel_hi:[1,0]
	v_pk_add_f32 v[34:35], v[34:35], s[96:97] op_sel_hi:[1,0]
	v_rcp_f32_e32 v32, v32
	v_rcp_f32_e32 v33, v33
	v_rcp_f32_e32 v34, v34
	v_rcp_f32_e32 v35, v35
	v_pk_mul_f32 v[36:37], v[36:37], v[32:33]
	v_pk_mul_f32 v[38:39], v[38:39], v[34:35]
	v_pk_fma_f32 v[32:33], v[98:99], s[90:91], v[250:251] op_sel_hi:[1,0,1]
	v_pk_fma_f32 v[34:35], v[100:101], s[90:91], v[252:253] op_sel_hi:[1,0,1]
	v_med3_f32 v32, v32, s79, v224
	v_med3_f32 v33, v33, s79, v224
	v_med3_f32 v34, v34, s79, v224
	v_med3_f32 v35, v35, s79, v224
	v_fma_f32 v32, v32, 4.0, 4.0
	v_fma_f32 v33, v33, 4.0, 4.0
	v_fma_f32 v34, v34, 4.0, 4.0
	v_fma_f32 v35, v35, 4.0, 4.0
	v_pk_mul_f32 v[36:37], v[32:33], v[36:37]
	v_pk_mul_f32 v[38:39], v[34:35], v[38:39]
	v_add_co_u32_e32 v22, vcc, s81, v18
	s_nop 0
	v_addc_co_u32_e32 v23, vcc, 0, v19, vcc
	v_mov_b32_e32 v20, v201
	v_mov_b32_e32 v21, v201
	v_cvt_pk_fp8_f32 v20, v28, v29
	v_cvt_pk_fp8_f32 v21, v36, v37
	v_cvt_pk_fp8_f32 v20, v30, v31 op_sel:[0,0,1]
	v_cvt_pk_fp8_f32 v21, v38, v39 op_sel:[0,0,1]
	global_store_dwordx2 v[22:23], v[20:21], off
	v_pk_fma_f32 v[28:29], v[94:95], s[90:91], v[238:239] op_sel_hi:[1,0,1]
	v_pk_fma_f32 v[30:31], v[96:97], s[90:91], v[240:241] op_sel_hi:[1,0,1]
	v_min_f32_e32 v28, 0x40e00000, v28
	v_min_f32_e32 v29, 0x40e00000, v29
	v_min_f32_e32 v30, 0x40e00000, v30
	v_min_f32_e32 v31, 0x40e00000, v31
	v_pk_mul_f32 v[32:33], v[28:29], s[92:93] op_sel_hi:[1,0]
	v_pk_mul_f32 v[34:35], v[30:31], s[92:93] op_sel_hi:[1,0]
	v_exp_f32_e32 v32, v32
	v_exp_f32_e32 v33, v33
	v_exp_f32_e32 v34, v34
	v_exp_f32_e32 v35, v35
	v_pk_add_f32 v[32:33], v[32:33], s[96:97] op_sel_hi:[1,0]
	v_pk_add_f32 v[34:35], v[34:35], s[96:97] op_sel_hi:[1,0]
	v_rcp_f32_e32 v32, v32
	v_rcp_f32_e32 v33, v33
	v_rcp_f32_e32 v34, v34
	v_rcp_f32_e32 v35, v35
	v_pk_mul_f32 v[28:29], v[28:29], v[32:33]
	v_pk_mul_f32 v[30:31], v[30:31], v[34:35]
	v_pk_fma_f32 v[32:33], v[90:91], s[90:91], v[246:247] op_sel_hi:[1,0,1]
	v_pk_fma_f32 v[34:35], v[92:93], s[90:91], v[248:249] op_sel_hi:[1,0,1]
	v_med3_f32 v32, v32, s79, v224
	v_med3_f32 v33, v33, s79, v224
	v_med3_f32 v34, v34, s79, v224
	v_med3_f32 v35, v35, s79, v224
	v_fma_f32 v32, v32, 4.0, 4.0
	v_fma_f32 v33, v33, 4.0, 4.0
	v_fma_f32 v34, v34, 4.0, 4.0
	v_fma_f32 v35, v35, 4.0, 4.0
	v_pk_mul_f32 v[28:29], v[32:33], v[28:29]
	v_pk_mul_f32 v[30:31], v[34:35], v[30:31]
	v_pk_fma_f32 v[36:37], v[86:87], s[90:91], v[242:243] op_sel_hi:[1,0,1]
	v_pk_fma_f32 v[38:39], v[88:89], s[90:91], v[244:245] op_sel_hi:[1,0,1]
	v_min_f32_e32 v36, 0x40e00000, v36
	v_min_f32_e32 v37, 0x40e00000, v37
	v_min_f32_e32 v38, 0x40e00000, v38
	v_min_f32_e32 v39, 0x40e00000, v39
	v_pk_mul_f32 v[32:33], v[36:37], s[92:93] op_sel_hi:[1,0]
	v_pk_mul_f32 v[34:35], v[38:39], s[92:93] op_sel_hi:[1,0]
	v_exp_f32_e32 v32, v32
	v_exp_f32_e32 v33, v33
	v_exp_f32_e32 v34, v34
	v_exp_f32_e32 v35, v35
	v_pk_add_f32 v[32:33], v[32:33], s[96:97] op_sel_hi:[1,0]
	v_pk_add_f32 v[34:35], v[34:35], s[96:97] op_sel_hi:[1,0]
	v_rcp_f32_e32 v32, v32
	v_rcp_f32_e32 v33, v33
	v_rcp_f32_e32 v34, v34
	v_rcp_f32_e32 v35, v35
	v_pk_mul_f32 v[36:37], v[36:37], v[32:33]
	v_pk_mul_f32 v[38:39], v[38:39], v[34:35]
	v_pk_fma_f32 v[32:33], v[82:83], s[90:91], v[250:251] op_sel_hi:[1,0,1]
	v_pk_fma_f32 v[34:35], v[84:85], s[90:91], v[252:253] op_sel_hi:[1,0,1]
	v_med3_f32 v32, v32, s79, v224
	v_med3_f32 v33, v33, s79, v224
	v_med3_f32 v34, v34, s79, v224
	v_med3_f32 v35, v35, s79, v224
	v_fma_f32 v32, v32, 4.0, 4.0
	v_fma_f32 v33, v33, 4.0, 4.0
	v_fma_f32 v34, v34, 4.0, 4.0
	v_fma_f32 v35, v35, 4.0, 4.0
	v_pk_mul_f32 v[36:37], v[32:33], v[36:37]
	v_pk_mul_f32 v[38:39], v[34:35], v[38:39]
	v_add_co_u32_e32 v22, vcc, s82, v18
	s_nop 0
	v_addc_co_u32_e32 v23, vcc, 0, v19, vcc
	v_mov_b32_e32 v20, v201
	v_mov_b32_e32 v21, v201
	v_cvt_pk_fp8_f32 v20, v28, v29
	v_cvt_pk_fp8_f32 v21, v36, v37
	v_cvt_pk_fp8_f32 v20, v30, v31 op_sel:[0,0,1]
	v_cvt_pk_fp8_f32 v21, v38, v39 op_sel:[0,0,1]
	global_store_dwordx2 v[22:23], v[20:21], off
	v_pk_fma_f32 v[28:29], v[78:79], s[90:91], v[238:239] op_sel_hi:[1,0,1]
	v_pk_fma_f32 v[30:31], v[80:81], s[90:91], v[240:241] op_sel_hi:[1,0,1]
	v_min_f32_e32 v28, 0x40e00000, v28
	v_min_f32_e32 v29, 0x40e00000, v29
	v_min_f32_e32 v30, 0x40e00000, v30
	v_min_f32_e32 v31, 0x40e00000, v31
	v_pk_mul_f32 v[32:33], v[28:29], s[92:93] op_sel_hi:[1,0]
	v_pk_mul_f32 v[34:35], v[30:31], s[92:93] op_sel_hi:[1,0]
	v_exp_f32_e32 v32, v32
	v_exp_f32_e32 v33, v33
	v_exp_f32_e32 v34, v34
	v_exp_f32_e32 v35, v35
	v_pk_add_f32 v[32:33], v[32:33], s[96:97] op_sel_hi:[1,0]
	v_pk_add_f32 v[34:35], v[34:35], s[96:97] op_sel_hi:[1,0]
	v_rcp_f32_e32 v32, v32
	v_rcp_f32_e32 v33, v33
	v_rcp_f32_e32 v34, v34
	v_rcp_f32_e32 v35, v35
	v_pk_mul_f32 v[28:29], v[28:29], v[32:33]
	v_pk_mul_f32 v[30:31], v[30:31], v[34:35]
	v_pk_fma_f32 v[32:33], v[74:75], s[90:91], v[246:247] op_sel_hi:[1,0,1]
	v_pk_fma_f32 v[34:35], v[76:77], s[90:91], v[248:249] op_sel_hi:[1,0,1]
	v_med3_f32 v32, v32, s79, v224
	v_med3_f32 v33, v33, s79, v224
	v_med3_f32 v34, v34, s79, v224
	v_med3_f32 v35, v35, s79, v224
	v_fma_f32 v32, v32, 4.0, 4.0
	v_fma_f32 v33, v33, 4.0, 4.0
	v_fma_f32 v34, v34, 4.0, 4.0
	v_fma_f32 v35, v35, 4.0, 4.0
	v_pk_mul_f32 v[28:29], v[32:33], v[28:29]
	v_pk_mul_f32 v[30:31], v[34:35], v[30:31]
	v_pk_fma_f32 v[36:37], v[70:71], s[90:91], v[242:243] op_sel_hi:[1,0,1]
	v_pk_fma_f32 v[38:39], v[72:73], s[90:91], v[244:245] op_sel_hi:[1,0,1]
	v_min_f32_e32 v36, 0x40e00000, v36
	v_min_f32_e32 v37, 0x40e00000, v37
	v_min_f32_e32 v38, 0x40e00000, v38
	v_min_f32_e32 v39, 0x40e00000, v39
	v_pk_mul_f32 v[32:33], v[36:37], s[92:93] op_sel_hi:[1,0]
	v_pk_mul_f32 v[34:35], v[38:39], s[92:93] op_sel_hi:[1,0]
	v_exp_f32_e32 v32, v32
	v_exp_f32_e32 v33, v33
	v_exp_f32_e32 v34, v34
	v_exp_f32_e32 v35, v35
	v_pk_add_f32 v[32:33], v[32:33], s[96:97] op_sel_hi:[1,0]
	v_pk_add_f32 v[34:35], v[34:35], s[96:97] op_sel_hi:[1,0]
	v_rcp_f32_e32 v32, v32
	v_rcp_f32_e32 v33, v33
	v_rcp_f32_e32 v34, v34
	v_rcp_f32_e32 v35, v35
	v_pk_mul_f32 v[36:37], v[36:37], v[32:33]
	v_pk_mul_f32 v[38:39], v[38:39], v[34:35]
	v_pk_fma_f32 v[32:33], v[66:67], s[90:91], v[250:251] op_sel_hi:[1,0,1]
	v_pk_fma_f32 v[34:35], v[68:69], s[90:91], v[252:253] op_sel_hi:[1,0,1]
	v_med3_f32 v32, v32, s79, v224
	v_med3_f32 v33, v33, s79, v224
	v_med3_f32 v34, v34, s79, v224
	v_med3_f32 v35, v35, s79, v224
	v_fma_f32 v32, v32, 4.0, 4.0
	v_fma_f32 v33, v33, 4.0, 4.0
	v_fma_f32 v34, v34, 4.0, 4.0
	v_fma_f32 v35, v35, 4.0, 4.0
	v_pk_mul_f32 v[36:37], v[32:33], v[36:37]
	v_pk_mul_f32 v[38:39], v[34:35], v[38:39]
	v_add_co_u32_e32 v4, vcc, 0x58000, v18
	s_nop 1
	v_addc_co_u32_e32 v5, vcc, 0, v19, vcc
	s_and_b64 vcc, exec, s[4:5]
	s_mov_b64 s[4:5], -1
	v_mov_b32_e32 v2, v201
	v_mov_b32_e32 v3, v201
	v_cvt_pk_fp8_f32 v2, v28, v29
	v_cvt_pk_fp8_f32 v3, v36, v37
	v_cvt_pk_fp8_f32 v2, v30, v31 op_sel:[0,0,1]
	v_cvt_pk_fp8_f32 v3, v38, v39 op_sel:[0,0,1]
	global_store_dwordx2 v[4:5], v[2:3], off
	s_cbranch_vccnz .LBB0_2061
	s_andn2_b64 vcc, exec, s[20:21]
	s_cbranch_vccnz .LBB0_2060
	s_barrier
	s_branch .LBB0_2060
